# v69 + conv/pool staging: the 14 row loads of a tile issued together ahead of the tile barrier, one wait, then the LDS stores
# speedup vs baseline: 1.0072x; 1.0047x over previous
; #define LAS __attribute__((address_space(3)))
; __device__ __forceinline__ void ph_convpool_fast(const Args& a, LAS unsigned char* lds) {
;     ...
;     for (int tile = blockIdx.x; tile < M / 32; tile += gridDim.x) {
;         const int tok0 = tile * 32, t0 = tok0 & (T - 1);
;         __syncthreads();
;         for (int i = tid; i < 62 * 64; i += 512) { const int r = i >> 6, c8 = (i & 63) * 8; const int tt = t0 - 30 + r;
;             u32x4 v = (u32x4){0u, 0u, 0u, 0u}; if (tt >= 0) v = *(const u32x4*)(H0 + (size_t)(tok0 - 30 + r) * 1024 + 512 + c8);
;             *(LAS u32x4*)(lds + VT_OFF + r * 1024 + c8 * 2) = v; }
;         for (int i = tid; i < 47 * 64; i += 512) { const int r = i >> 6, c8 = (i & 63) * 8; const int tt = t0 - 15 + r;
;             u32x4 v = (u32x4){0u, 0u, 0u, 0u}; if (tt >= 0) v = *(const u32x4*)(H0 + (size_t)(tok0 - 15 + r) * 1024 + c8);
;             *(LAS u32x4*)(lds + UT_OFF + r * 1024 + c8 * 2) = v; }
;         __syncthreads();
.LBB0_270:
	s_lshl_b32 s0, s19, 5
	s_and_b32 s1, s0, 0x1fe0
	s_sub_i32 s11, 29, s1
	s_sub_i32 s10, s0, 30
	s_sub_i32 s20, 14, s1
	v_mov_b32_e32 v188, 0
	v_mov_b32_e32 v189, 0
	v_mov_b32_e32 v190, 0
	v_mov_b32_e32 v191, 0
	v_cmp_lt_i32_e32 vcc, s11, v138
	s_and_saveexec_b64 s[2:3], vcc
	v_add_u32_e32 v12, s10, v138
	v_ashrrev_i32_e32 v13, 31, v12
	v_lshlrev_b64 v[12:13], 11, v[12:13]
	v_lshl_add_u64 v[12:13], v[46:47], 0, v[12:13]
	global_load_dwordx4 v[188:191], v[12:13], off offset:1024
	s_mov_b64 exec, s[2:3]
	v_mov_b32_e32 v192, 0
	v_mov_b32_e32 v193, 0
	v_mov_b32_e32 v194, 0
	v_mov_b32_e32 v195, 0
	v_cmp_lt_i32_e32 vcc, s11, v146
	s_and_saveexec_b64 s[2:3], vcc
	v_add_u32_e32 v12, s10, v146
	v_ashrrev_i32_e32 v13, 31, v12
	v_lshlrev_b64 v[12:13], 11, v[12:13]
	v_lshl_add_u64 v[12:13], v[46:47], 0, v[12:13]
	global_load_dwordx4 v[192:195], v[12:13], off offset:1024
	s_mov_b64 exec, s[2:3]
	v_mov_b32_e32 v196, 0
	v_mov_b32_e32 v197, 0
	v_mov_b32_e32 v198, 0
	v_mov_b32_e32 v199, 0
	v_cmp_lt_i32_e32 vcc, s11, v141
	s_and_saveexec_b64 s[2:3], vcc
	v_add_u32_e32 v12, s10, v141
	v_ashrrev_i32_e32 v13, 31, v12
	v_lshlrev_b64 v[12:13], 11, v[12:13]
	v_lshl_add_u64 v[12:13], v[46:47], 0, v[12:13]
	global_load_dwordx4 v[196:199], v[12:13], off offset:1024
	s_mov_b64 exec, s[2:3]
	v_mov_b32_e32 v200, 0
	v_mov_b32_e32 v201, 0
	v_mov_b32_e32 v202, 0
	v_mov_b32_e32 v203, 0
	v_cmp_lt_i32_e32 vcc, s11, v147
	s_and_saveexec_b64 s[2:3], vcc
	v_add_u32_e32 v12, s10, v147
	v_ashrrev_i32_e32 v13, 31, v12
	v_lshlrev_b64 v[12:13], 11, v[12:13]
	v_lshl_add_u64 v[12:13], v[46:47], 0, v[12:13]
	global_load_dwordx4 v[200:203], v[12:13], off offset:1024
	s_mov_b64 exec, s[2:3]
	v_mov_b32_e32 v204, 0
	v_mov_b32_e32 v205, 0
	v_mov_b32_e32 v206, 0
	v_mov_b32_e32 v207, 0
	v_cmp_lt_i32_e32 vcc, s11, v142
	s_and_saveexec_b64 s[2:3], vcc
	v_add_u32_e32 v12, s10, v142
	v_ashrrev_i32_e32 v13, 31, v12
	v_lshlrev_b64 v[12:13], 11, v[12:13]
	v_lshl_add_u64 v[12:13], v[46:47], 0, v[12:13]
	global_load_dwordx4 v[204:207], v[12:13], off offset:1024
	s_mov_b64 exec, s[2:3]
	v_mov_b32_e32 v208, 0
	v_mov_b32_e32 v209, 0
	v_mov_b32_e32 v210, 0
	v_mov_b32_e32 v211, 0
	v_cmp_lt_i32_e32 vcc, s11, v148
	s_and_saveexec_b64 s[2:3], vcc
	v_add_u32_e32 v12, s10, v148
	v_ashrrev_i32_e32 v13, 31, v12
	v_lshlrev_b64 v[12:13], 11, v[12:13]
	v_lshl_add_u64 v[12:13], v[46:47], 0, v[12:13]
	global_load_dwordx4 v[208:211], v[12:13], off offset:1024
	s_mov_b64 exec, s[2:3]
	v_mov_b32_e32 v212, 0
	v_mov_b32_e32 v213, 0
	v_mov_b32_e32 v214, 0
	v_mov_b32_e32 v215, 0
	v_cmp_lt_i32_e32 vcc, s11, v149
	s_and_b64 vcc, vcc, s[4:5]
	s_and_saveexec_b64 s[2:3], vcc
	v_add_u32_e32 v12, s10, v149
	v_ashrrev_i32_e32 v13, 31, v12
	v_lshlrev_b64 v[12:13], 11, v[12:13]
	v_lshl_add_u64 v[12:13], v[46:47], 0, v[12:13]
	global_load_dwordx4 v[212:215], v[12:13], off offset:1024
	s_mov_b64 exec, s[2:3]
	v_mov_b32_e32 v216, 0
	v_mov_b32_e32 v217, 0
	v_mov_b32_e32 v218, 0
	v_mov_b32_e32 v219, 0
	v_cmp_lt_i32_e32 vcc, s11, v150
	s_and_b64 vcc, vcc, s[4:5]
	s_and_b64 vcc, vcc, s[6:7]
	s_and_saveexec_b64 s[2:3], vcc
	v_add_u32_e32 v12, s10, v150
	v_ashrrev_i32_e32 v13, 31, v12
	v_lshlrev_b64 v[12:13], 11, v[12:13]
	v_lshl_add_u64 v[12:13], v[46:47], 0, v[12:13]
	global_load_dwordx4 v[216:219], v[12:13], off offset:1024
	s_mov_b64 exec, s[2:3]
	v_mov_b32_e32 v220, 0
	v_mov_b32_e32 v221, 0
	v_mov_b32_e32 v222, 0
	v_mov_b32_e32 v223, 0
	v_mov_b32_e32 v16, v138
	v_cmp_lt_i32_e32 vcc, s20, v16
	s_and_saveexec_b64 s[2:3], vcc
	v_add3_u32 v12, s13, v16, -15
	v_ashrrev_i32_e32 v13, 31, v12
	v_lshlrev_b64 v[12:13], 11, v[12:13]
	v_lshl_add_u64 v[12:13], v[46:47], 0, v[12:13]
	global_load_dwordx4 v[220:223], v[12:13], off
	s_mov_b64 exec, s[2:3]
	v_mov_b32_e32 v224, 0
	v_mov_b32_e32 v225, 0
	v_mov_b32_e32 v226, 0
	v_mov_b32_e32 v227, 0
	v_add_u32_e32 v16, 8, v138
	v_cmp_lt_i32_e32 vcc, s20, v16
	v_add_u32_e32 v17, 0x200, v1
	v_cmp_le_u32_e64 s[8:9], v17, s15
	s_and_b64 vcc, vcc, s[8:9]
	s_and_saveexec_b64 s[2:3], vcc
	v_add3_u32 v12, s13, v16, -15
	v_ashrrev_i32_e32 v13, 31, v12
	v_lshlrev_b64 v[12:13], 11, v[12:13]
	v_lshl_add_u64 v[12:13], v[46:47], 0, v[12:13]
	global_load_dwordx4 v[224:227], v[12:13], off
	s_mov_b64 exec, s[2:3]
	v_mov_b32_e32 v228, 0
	v_mov_b32_e32 v229, 0
	v_mov_b32_e32 v230, 0
	v_mov_b32_e32 v231, 0
	v_add_u32_e32 v16, 16, v138
	v_cmp_lt_i32_e32 vcc, s20, v16
	v_add_u32_e32 v17, 0x400, v1
	v_cmp_le_u32_e64 s[8:9], v17, s15
	s_and_b64 vcc, vcc, s[8:9]
	s_and_saveexec_b64 s[2:3], vcc
	v_add3_u32 v12, s13, v16, -15
	v_ashrrev_i32_e32 v13, 31, v12
	v_lshlrev_b64 v[12:13], 11, v[12:13]
	v_lshl_add_u64 v[12:13], v[46:47], 0, v[12:13]
	global_load_dwordx4 v[228:231], v[12:13], off
	s_mov_b64 exec, s[2:3]
	v_mov_b32_e32 v232, 0
	v_mov_b32_e32 v233, 0
	v_mov_b32_e32 v234, 0
	v_mov_b32_e32 v235, 0
	v_add_u32_e32 v16, 24, v138
	v_cmp_lt_i32_e32 vcc, s20, v16
	v_add_u32_e32 v17, 0x600, v1
	v_cmp_le_u32_e64 s[8:9], v17, s15
	s_and_b64 vcc, vcc, s[8:9]
	s_and_saveexec_b64 s[2:3], vcc
	v_add3_u32 v12, s13, v16, -15
	v_ashrrev_i32_e32 v13, 31, v12
	v_lshlrev_b64 v[12:13], 11, v[12:13]
	v_lshl_add_u64 v[12:13], v[46:47], 0, v[12:13]
	global_load_dwordx4 v[232:235], v[12:13], off
	s_mov_b64 exec, s[2:3]
	v_mov_b32_e32 v236, 0
	v_mov_b32_e32 v237, 0
	v_mov_b32_e32 v238, 0
	v_mov_b32_e32 v239, 0
	v_add_u32_e32 v16, 32, v138
	v_cmp_lt_i32_e32 vcc, s20, v16
	v_add_u32_e32 v17, 0x800, v1
	v_cmp_le_u32_e64 s[8:9], v17, s15
	s_and_b64 vcc, vcc, s[8:9]
	s_and_saveexec_b64 s[2:3], vcc
	v_add3_u32 v12, s13, v16, -15
	v_ashrrev_i32_e32 v13, 31, v12
	v_lshlrev_b64 v[12:13], 11, v[12:13]
	v_lshl_add_u64 v[12:13], v[46:47], 0, v[12:13]
	global_load_dwordx4 v[236:239], v[12:13], off
	s_mov_b64 exec, s[2:3]
	v_mov_b32_e32 v240, 0
	v_mov_b32_e32 v241, 0
	v_mov_b32_e32 v242, 0
	v_mov_b32_e32 v243, 0
	v_add_u32_e32 v16, 40, v138
	v_cmp_lt_i32_e32 vcc, s20, v16
	v_add_u32_e32 v17, 0xa00, v1
	v_cmp_le_u32_e64 s[8:9], v17, s15
	s_and_b64 vcc, vcc, s[8:9]
	s_and_saveexec_b64 s[2:3], vcc
	v_add3_u32 v12, s13, v16, -15
	v_ashrrev_i32_e32 v13, 31, v12
	v_lshlrev_b64 v[12:13], 11, v[12:13]
	v_lshl_add_u64 v[12:13], v[46:47], 0, v[12:13]
	global_load_dwordx4 v[240:243], v[12:13], off
	s_mov_b64 exec, s[2:3]
	v_add_u32_e32 v12, v143, v139
	s_barrier
; #define LAS __attribute__((address_space(3)))
; __device__ __forceinline__ void ph_convpool_fast(const Args& a, LAS unsigned char* lds) {
;     ...
;         for (int i = tid; i < 62 * 64; i += 512) { const int r = i >> 6, c8 = (i & 63) * 8; const int tt = t0 - 30 + r;
;             u32x4 v = (u32x4){0u, 0u, 0u, 0u}; if (tt >= 0) v = *(const u32x4*)(H0 + (size_t)(tok0 - 30 + r) * 1024 + 512 + c8);
;             *(LAS u32x4*)(lds + VT_OFF + r * 1024 + c8 * 2) = v; }
;         for (int i = tid; i < 47 * 64; i += 512) { const int r = i >> 6, c8 = (i & 63) * 8; const int tt = t0 - 15 + r;
;             u32x4 v = (u32x4){0u, 0u, 0u, 0u}; if (tt >= 0) v = *(const u32x4*)(H0 + (size_t)(tok0 - 15 + r) * 1024 + c8);
;             *(LAS u32x4*)(lds + UT_OFF + r * 1024 + c8 * 2) = v; }
;         __syncthreads();
;         float acc[4][8];
; #pragma unroll
;         for (int j = 0; j < 4; ++j)
; #pragma unroll
;             for (int c = 0; c < 8; ++c) acc[j][c] = bias[c];
;         float wq[4][8];
; #pragma unroll
;         for (int q = 0; q < 4; ++q)
; #pragma unroll
;             for (int c = 0; c < 8; ++c) wq[q][c] = 0.f;
	s_waitcnt vmcnt(0)
	ds_write_b128 v12, v[188:191]
	ds_write_b128 v162, v[192:195]
	ds_write_b128 v163, v[196:199]
	ds_write_b128 v164, v[200:203]
	ds_write_b128 v165, v[204:207]
	ds_write_b128 v166, v[208:211]
	s_and_saveexec_b64 s[2:3], s[4:5]
	ds_write_b128 v167, v[212:215]
	s_and_b64 exec, exec, s[6:7]
	ds_write_b128 v168, v[216:219]
	s_mov_b64 exec, s[2:3]
	ds_write_b128 v152, v[220:223]
	v_add_u32_e32 v17, 0x200, v1
	v_cmp_le_u32_e64 s[8:9], v17, s15
	s_and_saveexec_b64 s[2:3], s[8:9]
	ds_write_b128 v152, v[224:227] offset:8192
	s_mov_b64 exec, s[2:3]
	v_add_u32_e32 v17, 0x400, v1
	v_cmp_le_u32_e64 s[8:9], v17, s15
	s_and_saveexec_b64 s[2:3], s[8:9]
	ds_write_b128 v152, v[228:231] offset:16384
	s_mov_b64 exec, s[2:3]
	v_add_u32_e32 v17, 0x600, v1
	v_cmp_le_u32_e64 s[8:9], v17, s15
	s_and_saveexec_b64 s[2:3], s[8:9]
	ds_write_b128 v152, v[232:235] offset:24576
	s_mov_b64 exec, s[2:3]
	v_add_u32_e32 v17, 0x800, v1
	v_cmp_le_u32_e64 s[8:9], v17, s15
	s_and_saveexec_b64 s[2:3], s[8:9]
	ds_write_b128 v152, v[236:239] offset:32768
	s_mov_b64 exec, s[2:3]
	v_add_u32_e32 v17, 0xa00, v1
	v_cmp_le_u32_e64 s[8:9], v17, s15
	s_and_saveexec_b64 s[2:3], s[8:9]
	ds_write_b128 v152, v[240:243] offset:40960
	s_mov_b64 exec, s[2:3]
	s_and_b32 s2, s13, 0x1fe0
	v_add_u32_e32 v12, s2, v145
	v_min_u32_e32 v12, v144, v12
	v_max_u32_e32 v174, 2, v12
	v_or_b32_e32 v12, s2, v44
	v_min_u32_e32 v12, v144, v12
	v_max_u32_e32 v175, 2, v12
	v_or_b32_e32 v12, s2, v42
	v_min_u32_e32 v12, v144, v12
	v_max_u32_e32 v177, 2, v12
	v_or_b32_e32 v12, s2, v40
	v_min_u32_e32 v12, v144, v12
	v_max_u32_e32 v179, 2, v12
	v_or_b32_e32 v12, s2, v44
	v_min_u32_e32 v12, v144, v12
	v_max_u32_e32 v176, 2, v12
	v_or_b32_e32 v12, s2, v42
	v_min_u32_e32 v12, v144, v12
	v_max_u32_e32 v178, 2, v12
	v_or_b32_e32 v12, s2, v40
	v_min_u32_e32 v12, v144, v12
	v_max_u32_e32 v180, 2, v12
	s_sub_i32 s10, 14, s1
.LBB0_293:
	v_mov_b32_e32 v92, 0
	s_mov_b32 s2, 3
	v_mov_b32_e32 v181, v153
	v_mov_b32_e32 v12, v23
	v_mov_b32_e32 v13, v25
	v_mov_b32_e32 v93, v92
	v_mov_b32_e32 v86, v92
	v_mov_b32_e32 v87, v92
	v_mov_b32_e32 v82, v92
	v_mov_b32_e32 v83, v92
	v_mov_b32_e32 v16, v22
	v_mov_b32_e32 v17, v24
	v_mov_b32_e32 v98, v92
	v_mov_b32_e32 v99, v92
	v_mov_b32_e32 v90, v92
	v_mov_b32_e32 v91, v92
	v_mov_b32_e32 v84, v92
	v_mov_b32_e32 v85, v92
	v_mov_b32_e32 v54, v19
	v_mov_b32_e32 v55, v21
	v_mov_b32_e32 v106, v92
	v_mov_b32_e32 v107, v92
	v_mov_b32_e32 v96, v92
	v_mov_b32_e32 v97, v92
	v_mov_b32_e32 v88, v92
	v_mov_b32_e32 v89, v92
	v_mov_b32_e32 v56, v18
	v_mov_b32_e32 v57, v20
	v_mov_b32_e32 v120, v92
	v_mov_b32_e32 v121, v92
	v_mov_b32_e32 v102, v92
	v_mov_b32_e32 v103, v92
	v_mov_b32_e32 v94, v92
	v_mov_b32_e32 v95, v92
	v_mov_b32_e32 v58, v23
	v_mov_b32_e32 v59, v25
	v_mov_b32_e32 v60, v22
	v_mov_b32_e32 v61, v24
	v_mov_b32_e32 v62, v19
	v_mov_b32_e32 v63, v21
	v_mov_b32_e32 v64, v18
	v_mov_b32_e32 v65, v20
	v_mov_b32_e32 v66, v23
	v_mov_b32_e32 v67, v25
	v_mov_b32_e32 v68, v22
	v_mov_b32_e32 v69, v24
	v_mov_b32_e32 v70, v19
	v_mov_b32_e32 v71, v21
	v_mov_b32_e32 v72, v18
	v_mov_b32_e32 v73, v20
	v_mov_b32_e32 v74, v23
	v_mov_b32_e32 v75, v25
	v_mov_b32_e32 v76, v22
	v_mov_b32_e32 v77, v24
	v_mov_b32_e32 v78, v19
	v_mov_b32_e32 v79, v21
	v_mov_b32_e32 v80, v18
	v_mov_b32_e32 v81, v20
	s_waitcnt lgkmcnt(0)
	s_barrier
	s_branch .LBB0_295
